# baseline (speedup 1.0000x reference)
.Lmk_start:
	s_mov_b32 s28, s8
	s_mov_b64 s[30:31], s[4:5]
	s_mov_b64 s[32:33], s[6:7]
	s_mov_b64 s[6:7], s[2:3]
	s_mov_b64 s[34:35], s[2:3]
	s_mov_b32 s2, s28
	s_and_b32 s3, s2, 7
	s_lshr_b32 s4, s2, 3
	s_and_b32 s5, s4, 3
	s_lshl_b32 s3, s3, 2
	s_or_b32 s8, s3, s5
	s_lshr_b32 s9, s4, 2
	v_lshrrev_b32_e32 v127, 6, v0
	v_and_b32_e32 v124, 63, v0
	v_lshlrev_b32_e32 v124, 4, v124
	v_add_u32_e32 v125, 0xf000, v124
	v_readfirstlane_b32 s12, v127
	v_mov_b32_e32 v120, 0
	v_mov_b32_e32 v121, 0
	v_mov_b32_e32 v122, 0
	v_mov_b32_e32 v123, 0
	s_lshl_b32 s13, s12, 10
	s_lshl_b32 s14, s9, 3
	s_add_u32 s14, s14, s12
	s_mul_i32 s15, s14, 0x1800
	s_mul_i32 s16, s8, 0x12000
	s_add_u32 s16, s16, 0xc0000
	s_add_u32 s16, s16, s13
	s_add_u32 s20, s13, 0x2000
	s_add_u32 s10, s6, s16
	s_addc_u32 s11, s7, 0
	s_add_u32 s18, s6, s15
	s_addc_u32 s19, s7, 0
	s_add_u32 s22, s18, 0xc00
	s_addc_u32 s23, s19, 0
	s_cmp_lt_u32 s12, 4
	s_cbranch_scc0 .Lmk_vb
	s_mov_b32 m0, s13
	s_nop 0
	global_load_lds_dwordx4 v124, s[10:11]
	s_add_u32 s26, s10, 0x2000
	s_addc_u32 s27, s11, 0
	s_mov_b32 m0, s20
	s_nop 0
	global_load_lds_dwordx4 v124, s[26:27]
	global_load_dwordx4 v[96:99], v124, s[18:19]
	global_load_dwordx4 v[100:103], v124, s[18:19] offset:1024
	global_load_dwordx4 v[104:107], v124, s[18:19] offset:2048
	global_load_dwordx4 v[108:111], v124, s[22:23]
	global_load_dwordx4 v[112:115], v124, s[22:23] offset:1024
	global_load_dwordx4 v[116:119], v124, s[22:23] offset:2048
	s_add_u32 s24, s10, 0x3000
	s_addc_u32 s25, s11, 0
	s_add_u32 s26, s13, 0x3000
	s_mov_b32 m0, s26
	s_nop 0
	global_load_lds_dwordx4 v124, s[24:25]
	s_add_u32 s26, s24, 0x2000
	s_addc_u32 s27, s25, 0
	s_add_u32 s29, s20, 0x3000
	s_mov_b32 m0, s29
	s_nop 0
	global_load_lds_dwordx4 v124, s[26:27]
	s_add_u32 s24, s10, 0x6000
	s_addc_u32 s25, s11, 0
	s_add_u32 s26, s13, 0x6000
	s_mov_b32 m0, s26
	s_nop 0
	global_load_lds_dwordx4 v124, s[24:25]
	s_add_u32 s26, s24, 0x2000
	s_addc_u32 s27, s25, 0
	s_add_u32 s29, s20, 0x6000
	s_mov_b32 m0, s29
	s_nop 0
	global_load_lds_dwordx4 v124, s[26:27]
	s_add_u32 s24, s10, 0x9000
	s_addc_u32 s25, s11, 0
	s_add_u32 s26, s13, 0x9000
	s_mov_b32 m0, s26
	s_nop 0
	global_load_lds_dwordx4 v124, s[24:25]
	s_add_u32 s26, s24, 0x2000
	s_addc_u32 s27, s25, 0
	s_add_u32 s29, s20, 0x9000
	s_mov_b32 m0, s29
	s_nop 0
	global_load_lds_dwordx4 v124, s[26:27]
	s_add_u32 s24, s10, 0xc000
	s_addc_u32 s25, s11, 0
	s_add_u32 s26, s13, 0xc000
	s_mov_b32 m0, s26
	s_nop 0
	global_load_lds_dwordx4 v124, s[24:25]
	s_add_u32 s26, s24, 0x2000
	s_addc_u32 s27, s25, 0
	s_add_u32 s29, s20, 0xc000
	s_mov_b32 m0, s29
	s_nop 0
	global_load_lds_dwordx4 v124, s[26:27]
	s_add_u32 s24, s10, 0xf000
	s_addc_u32 s25, s11, 0
	s_add_u32 s26, s13, 0xf000
	s_mov_b32 m0, s26
	s_nop 0
	global_load_lds_dwordx4 v124, s[24:25]
	s_add_u32 s26, s24, 0x2000
	s_addc_u32 s27, s25, 0
	s_add_u32 s29, s20, 0xf000
	s_mov_b32 m0, s29
	s_nop 0
	global_load_lds_dwordx4 v124, s[26:27]
	s_waitcnt vmcnt(10)
	s_barrier
	ds_read_b128 v[0:3], v124
	ds_read_b128 v[4:7], v124 offset:1024
	ds_read_b128 v[8:11], v124 offset:2048
	ds_read_b128 v[12:15], v124 offset:3072
	ds_read_b128 v[16:19], v124 offset:4096
	ds_read_b128 v[20:23], v124 offset:5120
	s_waitcnt lgkmcnt(0)
	s_setprio 2
	v_mfma_f32_32x32x64_f8f6f4 v[48:63], v[0:5], v[96:101], 0 cbsz:2 blgp:2
	ds_read_b128 v[24:27], v124 offset:6144
	v_mfma_f32_32x32x64_f8f6f4 v[48:63], v[6:11], v[102:107], v[48:63] cbsz:2 blgp:2
	ds_read_b128 v[28:31], v124 offset:7168
	ds_read_b128 v[32:35], v124 offset:8192
	v_mfma_f32_32x32x64_f8f6f4 v[48:63], v[12:17], v[108:113], v[48:63] cbsz:2 blgp:2
	ds_read_b128 v[36:39], v124 offset:9216
	v_mfma_f32_32x32x64_f8f6f4 v[48:63], v[18:23], v[114:119], v[48:63] cbsz:2 blgp:2
	ds_read_b128 v[40:43], v124 offset:10240
	ds_read_b128 v[44:47], v124 offset:11264
	s_waitcnt vmcnt(0) lgkmcnt(0)
	s_barrier
	v_mfma_f32_32x32x64_f8f6f4 v[64:79], v[24:29], v[96:101], 0 cbsz:2 blgp:2
	ds_read_b128 v[0:3], v124 offset:12288
	ds_read_b128 v[4:7], v124 offset:13312
	ds_read_b128 v[8:11], v124 offset:14336
	ds_read_b128 v[24:27], v124 offset:18432
	v_mfma_f32_32x32x64_f8f6f4 v[64:79], v[30:35], v[102:107], v[64:79] cbsz:2 blgp:2
	ds_read_b128 v[12:15], v124 offset:15360
	ds_read_b128 v[16:19], v124 offset:16384
	ds_read_b128 v[20:23], v124 offset:17408
	ds_read_b128 v[28:31], v124 offset:19456
	ds_read_b128 v[32:35], v124 offset:20480
	v_exp_f32_e32 v48, v48
	v_exp_f32_e32 v49, v49
	v_exp_f32_e32 v50, v50
	v_exp_f32_e32 v51, v51
	v_mfma_f32_32x32x64_f8f6f4 v[64:79], v[36:41], v[108:113], v[64:79] cbsz:2 blgp:2
	ds_read_b128 v[36:39], v124 offset:21504
	v_exp_f32_e32 v52, v52
	v_exp_f32_e32 v53, v53
	v_exp_f32_e32 v54, v54
	v_exp_f32_e32 v55, v55
	v_pk_add_f32 v[120:121], v[120:121], v[48:49]
	v_pk_add_f32 v[122:123], v[122:123], v[50:51]
	v_mfma_f32_32x32x64_f8f6f4 v[64:79], v[42:47], v[114:119], v[64:79] cbsz:2 blgp:2
	ds_read_b128 v[40:43], v124 offset:22528
	ds_read_b128 v[44:47], v124 offset:23552
	v_exp_f32_e32 v56, v56
	v_exp_f32_e32 v57, v57
	v_exp_f32_e32 v58, v58
	v_exp_f32_e32 v59, v59
	v_pk_add_f32 v[120:121], v[120:121], v[52:53]
	v_pk_add_f32 v[122:123], v[122:123], v[54:55]
	s_waitcnt lgkmcnt(5)
	v_mfma_f32_32x32x64_f8f6f4 v[80:95], v[0:5], v[96:101], 0 cbsz:2 blgp:2
	ds_read_b128 v[0:3], v124 offset:24576
	v_exp_f32_e32 v60, v60
	v_exp_f32_e32 v61, v61
	v_exp_f32_e32 v62, v62
	v_exp_f32_e32 v63, v63
	v_pk_add_f32 v[120:121], v[120:121], v[56:57]
	v_pk_add_f32 v[122:123], v[122:123], v[58:59]
	v_mfma_f32_32x32x64_f8f6f4 v[80:95], v[6:11], v[102:107], v[80:95] cbsz:2 blgp:2
	ds_read_b128 v[4:7], v124 offset:25600
	ds_read_b128 v[8:11], v124 offset:26624
	v_exp_f32_e32 v64, v64
	v_exp_f32_e32 v65, v65
	v_exp_f32_e32 v66, v66
	v_exp_f32_e32 v67, v67
	v_pk_add_f32 v[120:121], v[120:121], v[60:61]
	v_pk_add_f32 v[122:123], v[122:123], v[62:63]
	v_mfma_f32_32x32x64_f8f6f4 v[80:95], v[12:17], v[108:113], v[80:95] cbsz:2 blgp:2
	ds_read_b128 v[12:15], v124 offset:27648
	v_exp_f32_e32 v68, v68
	v_exp_f32_e32 v69, v69
	v_exp_f32_e32 v70, v70
	v_exp_f32_e32 v71, v71
	v_pk_add_f32 v[120:121], v[120:121], v[64:65]
	v_pk_add_f32 v[122:123], v[122:123], v[66:67]
	v_mfma_f32_32x32x64_f8f6f4 v[80:95], v[18:23], v[114:119], v[80:95] cbsz:2 blgp:2
	ds_read_b128 v[16:19], v124 offset:28672
	ds_read_b128 v[20:23], v124 offset:29696
	v_exp_f32_e32 v72, v72
	v_exp_f32_e32 v73, v73
	v_exp_f32_e32 v74, v74
	v_exp_f32_e32 v75, v75
	v_pk_add_f32 v[120:121], v[120:121], v[68:69]
	v_pk_add_f32 v[122:123], v[122:123], v[70:71]
	s_waitcnt lgkmcnt(6)
	v_mfma_f32_32x32x64_f8f6f4 v[48:63], v[24:29], v[96:101], 0 cbsz:2 blgp:2
	ds_read_b128 v[24:27], v124 offset:30720
	v_exp_f32_e32 v76, v76
	v_exp_f32_e32 v77, v77
	v_exp_f32_e32 v78, v78
	v_exp_f32_e32 v79, v79
	v_pk_add_f32 v[120:121], v[120:121], v[72:73]
	v_pk_add_f32 v[122:123], v[122:123], v[74:75]
	v_mfma_f32_32x32x64_f8f6f4 v[48:63], v[30:35], v[102:107], v[48:63] cbsz:2 blgp:2
	ds_read_b128 v[28:31], v124 offset:31744
	ds_read_b128 v[32:35], v124 offset:32768
	v_exp_f32_e32 v80, v80
	v_exp_f32_e32 v81, v81
	v_exp_f32_e32 v82, v82
	v_exp_f32_e32 v83, v83
	v_pk_add_f32 v[120:121], v[120:121], v[76:77]
	v_pk_add_f32 v[122:123], v[122:123], v[78:79]
	v_mfma_f32_32x32x64_f8f6f4 v[48:63], v[36:41], v[108:113], v[48:63] cbsz:2 blgp:2
	ds_read_b128 v[36:39], v124 offset:33792
	v_exp_f32_e32 v84, v84
	v_exp_f32_e32 v85, v85
	v_exp_f32_e32 v86, v86
	v_exp_f32_e32 v87, v87
	v_pk_add_f32 v[120:121], v[120:121], v[80:81]
	v_pk_add_f32 v[122:123], v[122:123], v[82:83]
	v_mfma_f32_32x32x64_f8f6f4 v[48:63], v[42:47], v[114:119], v[48:63] cbsz:2 blgp:2
	ds_read_b128 v[40:43], v124 offset:34816
	ds_read_b128 v[44:47], v124 offset:35840
	v_exp_f32_e32 v88, v88
	v_exp_f32_e32 v89, v89
	v_exp_f32_e32 v90, v90
	v_exp_f32_e32 v91, v91
	v_pk_add_f32 v[120:121], v[120:121], v[84:85]
	v_pk_add_f32 v[122:123], v[122:123], v[86:87]
	s_setprio 1
	s_waitcnt lgkmcnt(6)
	v_mfma_f32_32x32x64_f8f6f4 v[64:79], v[0:5], v[96:101], 0 cbsz:2 blgp:2
	ds_read_b128 v[0:3], v124 offset:36864
	v_exp_f32_e32 v92, v92
	v_exp_f32_e32 v93, v93
	v_exp_f32_e32 v94, v94
	v_exp_f32_e32 v95, v95
	v_pk_add_f32 v[120:121], v[120:121], v[88:89]
	v_pk_add_f32 v[122:123], v[122:123], v[90:91]
	v_mfma_f32_32x32x64_f8f6f4 v[64:79], v[6:11], v[102:107], v[64:79] cbsz:2 blgp:2
	ds_read_b128 v[4:7], v124 offset:37888
	ds_read_b128 v[8:11], v124 offset:38912
	v_exp_f32_e32 v48, v48
	v_exp_f32_e32 v49, v49
	v_exp_f32_e32 v50, v50
	v_exp_f32_e32 v51, v51
	v_pk_add_f32 v[120:121], v[120:121], v[92:93]
	v_pk_add_f32 v[122:123], v[122:123], v[94:95]
	v_mfma_f32_32x32x64_f8f6f4 v[64:79], v[12:17], v[108:113], v[64:79] cbsz:2 blgp:2
	ds_read_b128 v[12:15], v124 offset:39936
	v_exp_f32_e32 v52, v52
	v_exp_f32_e32 v53, v53
	v_exp_f32_e32 v54, v54
	v_exp_f32_e32 v55, v55
	v_pk_add_f32 v[120:121], v[120:121], v[48:49]
	v_pk_add_f32 v[122:123], v[122:123], v[50:51]
	v_mfma_f32_32x32x64_f8f6f4 v[64:79], v[18:23], v[114:119], v[64:79] cbsz:2 blgp:2
	ds_read_b128 v[16:19], v124 offset:40960
	ds_read_b128 v[20:23], v124 offset:41984
	v_exp_f32_e32 v56, v56
	v_exp_f32_e32 v57, v57
	v_exp_f32_e32 v58, v58
	v_exp_f32_e32 v59, v59
	v_pk_add_f32 v[120:121], v[120:121], v[52:53]
	v_pk_add_f32 v[122:123], v[122:123], v[54:55]
	s_waitcnt lgkmcnt(6)
	v_mfma_f32_32x32x64_f8f6f4 v[80:95], v[24:29], v[96:101], 0 cbsz:2 blgp:2
	ds_read_b128 v[24:27], v124 offset:43008
	v_exp_f32_e32 v60, v60
	v_exp_f32_e32 v61, v61
	v_exp_f32_e32 v62, v62
	v_exp_f32_e32 v63, v63
	v_pk_add_f32 v[120:121], v[120:121], v[56:57]
	v_pk_add_f32 v[122:123], v[122:123], v[58:59]
	v_mfma_f32_32x32x64_f8f6f4 v[80:95], v[30:35], v[102:107], v[80:95] cbsz:2 blgp:2
	ds_read_b128 v[28:31], v124 offset:44032
	ds_read_b128 v[32:35], v124 offset:45056
	v_exp_f32_e32 v64, v64
	v_exp_f32_e32 v65, v65
	v_exp_f32_e32 v66, v66
	v_exp_f32_e32 v67, v67
	v_pk_add_f32 v[120:121], v[120:121], v[60:61]
	v_pk_add_f32 v[122:123], v[122:123], v[62:63]
	v_mfma_f32_32x32x64_f8f6f4 v[80:95], v[36:41], v[108:113], v[80:95] cbsz:2 blgp:2
	ds_read_b128 v[36:39], v124 offset:46080
	v_exp_f32_e32 v68, v68
	v_exp_f32_e32 v69, v69
	v_exp_f32_e32 v70, v70
	v_exp_f32_e32 v71, v71
	v_pk_add_f32 v[120:121], v[120:121], v[64:65]
	v_pk_add_f32 v[122:123], v[122:123], v[66:67]
	v_mfma_f32_32x32x64_f8f6f4 v[80:95], v[42:47], v[114:119], v[80:95] cbsz:2 blgp:2
	ds_read_b128 v[40:43], v124 offset:47104
	ds_read_b128 v[44:47], v124 offset:48128
	v_exp_f32_e32 v72, v72
	v_exp_f32_e32 v73, v73
	v_exp_f32_e32 v74, v74
	v_exp_f32_e32 v75, v75
	v_pk_add_f32 v[120:121], v[120:121], v[68:69]
	v_pk_add_f32 v[122:123], v[122:123], v[70:71]
	s_waitcnt lgkmcnt(6)
	v_mfma_f32_32x32x64_f8f6f4 v[48:63], v[0:5], v[96:101], 0 cbsz:2 blgp:2
	ds_read_b128 v[0:3], v124 offset:49152
	v_exp_f32_e32 v76, v76
	v_exp_f32_e32 v77, v77
	v_exp_f32_e32 v78, v78
	v_exp_f32_e32 v79, v79
	v_pk_add_f32 v[120:121], v[120:121], v[72:73]
	v_pk_add_f32 v[122:123], v[122:123], v[74:75]
	v_mfma_f32_32x32x64_f8f6f4 v[48:63], v[6:11], v[102:107], v[48:63] cbsz:2 blgp:2
	ds_read_b128 v[4:7], v124 offset:50176
	ds_read_b128 v[8:11], v124 offset:51200
	v_exp_f32_e32 v80, v80
	v_exp_f32_e32 v81, v81
	v_exp_f32_e32 v82, v82
	v_exp_f32_e32 v83, v83
	v_pk_add_f32 v[120:121], v[120:121], v[76:77]
	v_pk_add_f32 v[122:123], v[122:123], v[78:79]
	v_mfma_f32_32x32x64_f8f6f4 v[48:63], v[12:17], v[108:113], v[48:63] cbsz:2 blgp:2
	ds_read_b128 v[12:15], v124 offset:52224
	v_exp_f32_e32 v84, v84
	v_exp_f32_e32 v85, v85
	v_exp_f32_e32 v86, v86
	v_exp_f32_e32 v87, v87
	v_pk_add_f32 v[120:121], v[120:121], v[80:81]
	v_pk_add_f32 v[122:123], v[122:123], v[82:83]
	v_mfma_f32_32x32x64_f8f6f4 v[48:63], v[18:23], v[114:119], v[48:63] cbsz:2 blgp:2
	ds_read_b128 v[16:19], v124 offset:53248
	ds_read_b128 v[20:23], v124 offset:54272
	v_exp_f32_e32 v88, v88
	v_exp_f32_e32 v89, v89
	v_exp_f32_e32 v90, v90
	v_exp_f32_e32 v91, v91
	v_pk_add_f32 v[120:121], v[120:121], v[84:85]
	v_pk_add_f32 v[122:123], v[122:123], v[86:87]
	s_waitcnt lgkmcnt(6)
	v_mfma_f32_32x32x64_f8f6f4 v[64:79], v[24:29], v[96:101], 0 cbsz:2 blgp:2
	ds_read_b128 v[24:27], v124 offset:55296
	v_exp_f32_e32 v92, v92
	v_exp_f32_e32 v93, v93
	v_exp_f32_e32 v94, v94
	v_exp_f32_e32 v95, v95
	v_pk_add_f32 v[120:121], v[120:121], v[88:89]
	v_pk_add_f32 v[122:123], v[122:123], v[90:91]
	v_mfma_f32_32x32x64_f8f6f4 v[64:79], v[30:35], v[102:107], v[64:79] cbsz:2 blgp:2
	ds_read_b128 v[28:31], v124 offset:56320
	ds_read_b128 v[32:35], v124 offset:57344
	v_exp_f32_e32 v48, v48
	v_exp_f32_e32 v49, v49
	v_exp_f32_e32 v50, v50
	v_exp_f32_e32 v51, v51
	v_pk_add_f32 v[120:121], v[120:121], v[92:93]
	v_pk_add_f32 v[122:123], v[122:123], v[94:95]
	v_mfma_f32_32x32x64_f8f6f4 v[64:79], v[36:41], v[108:113], v[64:79] cbsz:2 blgp:2
	ds_read_b128 v[36:39], v124 offset:58368
	v_exp_f32_e32 v52, v52
	v_exp_f32_e32 v53, v53
	v_exp_f32_e32 v54, v54
	v_exp_f32_e32 v55, v55
	v_pk_add_f32 v[120:121], v[120:121], v[48:49]
	v_pk_add_f32 v[122:123], v[122:123], v[50:51]
	v_mfma_f32_32x32x64_f8f6f4 v[64:79], v[42:47], v[114:119], v[64:79] cbsz:2 blgp:2
	ds_read_b128 v[40:43], v124 offset:59392
	ds_read_b128 v[44:47], v124 offset:60416
	v_exp_f32_e32 v56, v56
	v_exp_f32_e32 v57, v57
	v_exp_f32_e32 v58, v58
	v_exp_f32_e32 v59, v59
	v_pk_add_f32 v[120:121], v[120:121], v[52:53]
	v_pk_add_f32 v[122:123], v[122:123], v[54:55]
	s_setprio 0
	s_waitcnt lgkmcnt(6)
	v_mfma_f32_32x32x64_f8f6f4 v[80:95], v[0:5], v[96:101], 0 cbsz:2 blgp:2
	ds_read_b128 v[0:3], v125
	v_exp_f32_e32 v60, v60
	v_exp_f32_e32 v61, v61
	v_exp_f32_e32 v62, v62
	v_exp_f32_e32 v63, v63
	v_pk_add_f32 v[120:121], v[120:121], v[56:57]
	v_pk_add_f32 v[122:123], v[122:123], v[58:59]
	v_mfma_f32_32x32x64_f8f6f4 v[80:95], v[6:11], v[102:107], v[80:95] cbsz:2 blgp:2
	ds_read_b128 v[4:7], v125 offset:1024
	ds_read_b128 v[8:11], v125 offset:2048
	v_exp_f32_e32 v64, v64
	v_exp_f32_e32 v65, v65
	v_exp_f32_e32 v66, v66
	v_exp_f32_e32 v67, v67
	v_pk_add_f32 v[120:121], v[120:121], v[60:61]
	v_pk_add_f32 v[122:123], v[122:123], v[62:63]
	v_mfma_f32_32x32x64_f8f6f4 v[80:95], v[12:17], v[108:113], v[80:95] cbsz:2 blgp:2
	ds_read_b128 v[12:15], v125 offset:3072
	v_exp_f32_e32 v68, v68
	v_exp_f32_e32 v69, v69
	v_exp_f32_e32 v70, v70
	v_exp_f32_e32 v71, v71
	v_pk_add_f32 v[120:121], v[120:121], v[64:65]
	v_pk_add_f32 v[122:123], v[122:123], v[66:67]
	v_mfma_f32_32x32x64_f8f6f4 v[80:95], v[18:23], v[114:119], v[80:95] cbsz:2 blgp:2
	ds_read_b128 v[16:19], v125 offset:4096
	ds_read_b128 v[20:23], v125 offset:5120
	v_exp_f32_e32 v72, v72
	v_exp_f32_e32 v73, v73
	v_exp_f32_e32 v74, v74
	v_exp_f32_e32 v75, v75
	v_pk_add_f32 v[120:121], v[120:121], v[68:69]
	v_pk_add_f32 v[122:123], v[122:123], v[70:71]
	s_waitcnt lgkmcnt(6)
	v_mfma_f32_32x32x64_f8f6f4 v[48:63], v[24:29], v[96:101], 0 cbsz:2 blgp:2
	ds_read_b128 v[24:27], v125 offset:6144
	v_exp_f32_e32 v76, v76
	v_exp_f32_e32 v77, v77
	v_exp_f32_e32 v78, v78
	v_exp_f32_e32 v79, v79
	v_pk_add_f32 v[120:121], v[120:121], v[72:73]
	v_pk_add_f32 v[122:123], v[122:123], v[74:75]
	v_mfma_f32_32x32x64_f8f6f4 v[48:63], v[30:35], v[102:107], v[48:63] cbsz:2 blgp:2
	ds_read_b128 v[28:31], v125 offset:7168
	ds_read_b128 v[32:35], v125 offset:8192
	v_exp_f32_e32 v80, v80
	v_exp_f32_e32 v81, v81
	v_exp_f32_e32 v82, v82
	v_exp_f32_e32 v83, v83
	v_pk_add_f32 v[120:121], v[120:121], v[76:77]
	v_pk_add_f32 v[122:123], v[122:123], v[78:79]
	s_cmp_lg_u32 s8, 10
	s_cbranch_scc1 .Lmk_nosplit_a
	v_add_f32_e32 v127, v120, v121
	v_add_f32_e32 v126, v122, v123
	v_mov_b32_e32 v120, 0
	v_mov_b32_e32 v121, 0
	v_mov_b32_e32 v122, 0
	v_mov_b32_e32 v123, 0
	v_add_f32_e32 v127, v127, v126
.Lmk_nosplit_a:
	v_mfma_f32_32x32x64_f8f6f4 v[48:63], v[36:41], v[108:113], v[48:63] cbsz:2 blgp:2
	ds_read_b128 v[36:39], v125 offset:9216
	v_exp_f32_e32 v84, v84
	v_exp_f32_e32 v85, v85
	v_exp_f32_e32 v86, v86
	v_exp_f32_e32 v87, v87
	v_pk_add_f32 v[120:121], v[120:121], v[80:81]
	v_pk_add_f32 v[122:123], v[122:123], v[82:83]
	v_mfma_f32_32x32x64_f8f6f4 v[48:63], v[42:47], v[114:119], v[48:63] cbsz:2 blgp:2
	ds_read_b128 v[40:43], v125 offset:10240
	ds_read_b128 v[44:47], v125 offset:11264
	v_exp_f32_e32 v88, v88
	v_exp_f32_e32 v89, v89
	v_exp_f32_e32 v90, v90
	v_exp_f32_e32 v91, v91
	v_pk_add_f32 v[120:121], v[120:121], v[84:85]
	v_pk_add_f32 v[122:123], v[122:123], v[86:87]
	s_waitcnt lgkmcnt(6)
	v_mfma_f32_32x32x64_f8f6f4 v[64:79], v[0:5], v[96:101], 0 cbsz:2 blgp:2
	v_exp_f32_e32 v92, v92
	v_exp_f32_e32 v93, v93
	v_exp_f32_e32 v94, v94
	v_exp_f32_e32 v95, v95
	v_pk_add_f32 v[120:121], v[120:121], v[88:89]
	v_pk_add_f32 v[122:123], v[122:123], v[90:91]
	v_mfma_f32_32x32x64_f8f6f4 v[64:79], v[6:11], v[102:107], v[64:79] cbsz:2 blgp:2
	v_exp_f32_e32 v48, v48
	v_exp_f32_e32 v49, v49
	v_exp_f32_e32 v50, v50
	v_exp_f32_e32 v51, v51
	v_pk_add_f32 v[120:121], v[120:121], v[92:93]
	v_pk_add_f32 v[122:123], v[122:123], v[94:95]
	v_mfma_f32_32x32x64_f8f6f4 v[64:79], v[12:17], v[108:113], v[64:79] cbsz:2 blgp:2
	v_exp_f32_e32 v52, v52
	v_exp_f32_e32 v53, v53
	v_exp_f32_e32 v54, v54
	v_exp_f32_e32 v55, v55
	v_pk_add_f32 v[120:121], v[120:121], v[48:49]
	v_pk_add_f32 v[122:123], v[122:123], v[50:51]
	v_mfma_f32_32x32x64_f8f6f4 v[64:79], v[18:23], v[114:119], v[64:79] cbsz:2 blgp:2
	v_exp_f32_e32 v56, v56
	v_exp_f32_e32 v57, v57
	v_exp_f32_e32 v58, v58
	v_exp_f32_e32 v59, v59
	v_pk_add_f32 v[120:121], v[120:121], v[52:53]
	v_pk_add_f32 v[122:123], v[122:123], v[54:55]
	s_waitcnt lgkmcnt(0)
	v_mfma_f32_32x32x64_f8f6f4 v[80:95], v[24:29], v[96:101], 0 cbsz:2 blgp:2
	v_exp_f32_e32 v60, v60
	v_exp_f32_e32 v61, v61
	v_exp_f32_e32 v62, v62
	v_exp_f32_e32 v63, v63
	v_pk_add_f32 v[120:121], v[120:121], v[56:57]
	v_pk_add_f32 v[122:123], v[122:123], v[58:59]
	v_mfma_f32_32x32x64_f8f6f4 v[80:95], v[30:35], v[102:107], v[80:95] cbsz:2 blgp:2
	v_exp_f32_e32 v64, v64
	v_exp_f32_e32 v65, v65
	v_exp_f32_e32 v66, v66
	v_exp_f32_e32 v67, v67
	v_pk_add_f32 v[120:121], v[120:121], v[60:61]
	v_pk_add_f32 v[122:123], v[122:123], v[62:63]
	v_mfma_f32_32x32x64_f8f6f4 v[80:95], v[36:41], v[108:113], v[80:95] cbsz:2 blgp:2
	v_exp_f32_e32 v68, v68
	v_exp_f32_e32 v69, v69
	v_exp_f32_e32 v70, v70
	v_exp_f32_e32 v71, v71
	v_pk_add_f32 v[120:121], v[120:121], v[64:65]
	v_pk_add_f32 v[122:123], v[122:123], v[66:67]
	v_mfma_f32_32x32x64_f8f6f4 v[80:95], v[42:47], v[114:119], v[80:95] cbsz:2 blgp:2
	v_exp_f32_e32 v72, v72
	v_exp_f32_e32 v73, v73
	v_exp_f32_e32 v74, v74
	v_exp_f32_e32 v75, v75
	v_pk_add_f32 v[120:121], v[120:121], v[68:69]
	v_pk_add_f32 v[122:123], v[122:123], v[70:71]
	v_exp_f32_e32 v76, v76
	v_exp_f32_e32 v77, v77
	v_exp_f32_e32 v78, v78
	v_exp_f32_e32 v79, v79
	v_pk_add_f32 v[120:121], v[120:121], v[72:73]
	v_pk_add_f32 v[122:123], v[122:123], v[74:75]
	s_nop 1
	v_exp_f32_e32 v80, v80
	v_exp_f32_e32 v81, v81
	v_exp_f32_e32 v82, v82
	v_exp_f32_e32 v83, v83
	v_pk_add_f32 v[120:121], v[120:121], v[76:77]
	v_pk_add_f32 v[122:123], v[122:123], v[78:79]
	v_exp_f32_e32 v84, v84
	v_exp_f32_e32 v85, v85
	v_exp_f32_e32 v86, v86
	v_exp_f32_e32 v87, v87
	v_pk_add_f32 v[120:121], v[120:121], v[80:81]
	v_pk_add_f32 v[122:123], v[122:123], v[82:83]
	v_exp_f32_e32 v88, v88
	v_exp_f32_e32 v89, v89
	v_exp_f32_e32 v90, v90
	v_exp_f32_e32 v91, v91
	v_pk_add_f32 v[120:121], v[120:121], v[84:85]
	v_pk_add_f32 v[122:123], v[122:123], v[86:87]
	v_exp_f32_e32 v92, v92
	v_exp_f32_e32 v93, v93
	v_exp_f32_e32 v94, v94
	v_exp_f32_e32 v95, v95
	v_pk_add_f32 v[120:121], v[120:121], v[88:89]
	v_pk_add_f32 v[122:123], v[122:123], v[90:91]
	v_pk_add_f32 v[120:121], v[120:121], v[92:93]
	v_pk_add_f32 v[122:123], v[122:123], v[94:95]
	v_add_f32_e32 v120, v120, v121
	v_add_f32_e32 v122, v122, v123
	v_lshrrev_b32_e32 v126, 2, v124
	v_add_f32_e32 v120, v120, v122
	v_mov_b32_e32 v123, v127
	v_mov_b32_e32 v122, v120
	s_mov_b64 s[4:5], s[30:31]
	s_mov_b64 s[6:7], s[32:33]
	s_lshl_b32 s14, s14, 7
	v_add_u32_e32 v126, s14, v126
	s_nop 1
	v_permlane32_swap_b32_e32 v120, v122
	v_permlane32_swap_b32_e32 v127, v123
	s_nop 1
	v_add_f32_e32 v120, v120, v122
	v_add_f32_e32 v127, v127, v123
	v_cmp_gt_u32_e32 vcc, 0x200, v124
	s_and_saveexec_b64 s[16:17], vcc
	s_cbranch_execz .Lmk_end_a
	s_cmp_lt_u32 s8, 10
	s_cbranch_scc1 .Lmk_pos_only_a
	s_cmp_eq_u32 s8, 10
	s_cbranch_scc0 .Lmk_neg_only_a
	global_atomic_add_f32 v126, v127, s[4:5]

.Lmk_vb:
	s_mov_b32 m0, s13
	s_nop 0
	global_load_lds_dwordx4 v124, s[10:11]
	global_load_dwordx4 v[96:99], v124, s[18:19]
	global_load_dwordx4 v[100:103], v124, s[18:19] offset:1024
	global_load_dwordx4 v[104:107], v124, s[18:19] offset:2048
	global_load_dwordx4 v[108:111], v124, s[22:23]
	global_load_dwordx4 v[112:115], v124, s[22:23] offset:1024
	global_load_dwordx4 v[116:119], v124, s[22:23] offset:2048
	s_add_u32 s24, s10, 0x3000
	s_addc_u32 s25, s11, 0
	s_add_u32 s26, s13, 0x3000
	s_mov_b32 m0, s26
	s_nop 0
	global_load_lds_dwordx4 v124, s[24:25]
	s_add_u32 s24, s10, 0x6000
	s_addc_u32 s25, s11, 0
	s_add_u32 s26, s13, 0x6000
	s_mov_b32 m0, s26
	s_nop 0
	global_load_lds_dwordx4 v124, s[24:25]
	s_add_u32 s24, s10, 0x9000
	s_addc_u32 s25, s11, 0
	s_add_u32 s26, s13, 0x9000
	s_mov_b32 m0, s26
	s_nop 0
	global_load_lds_dwordx4 v124, s[24:25]
	s_add_u32 s24, s10, 0xc000
	s_addc_u32 s25, s11, 0
	s_add_u32 s26, s13, 0xc000
	s_mov_b32 m0, s26
	s_nop 0
	global_load_lds_dwordx4 v124, s[24:25]
	s_add_u32 s24, s10, 0xf000
	s_addc_u32 s25, s11, 0
	s_add_u32 s26, s13, 0xf000
	s_mov_b32 m0, s26
	s_nop 0
	global_load_lds_dwordx4 v124, s[24:25]
	s_waitcnt vmcnt(5)
	s_barrier
	ds_read_b128 v[0:3], v124
	ds_read_b128 v[4:7], v124 offset:1024
	ds_read_b128 v[8:11], v124 offset:2048
	ds_read_b128 v[12:15], v124 offset:3072
	ds_read_b128 v[16:19], v124 offset:4096
	ds_read_b128 v[20:23], v124 offset:5120
	s_waitcnt lgkmcnt(0)
	s_setprio 3
	v_mfma_f32_32x32x64_f8f6f4 v[48:63], v[0:5], v[96:101], 0 cbsz:2 blgp:2
	ds_read_b128 v[24:27], v124 offset:6144
	v_mfma_f32_32x32x64_f8f6f4 v[48:63], v[6:11], v[102:107], v[48:63] cbsz:2 blgp:2
	ds_read_b128 v[28:31], v124 offset:7168
	ds_read_b128 v[32:35], v124 offset:8192
	v_mfma_f32_32x32x64_f8f6f4 v[48:63], v[12:17], v[108:113], v[48:63] cbsz:2 blgp:2
	ds_read_b128 v[36:39], v124 offset:9216
	v_mfma_f32_32x32x64_f8f6f4 v[48:63], v[18:23], v[114:119], v[48:63] cbsz:2 blgp:2
	ds_read_b128 v[40:43], v124 offset:10240
	ds_read_b128 v[44:47], v124 offset:11264
	s_waitcnt vmcnt(0) lgkmcnt(0)
	s_barrier
	v_mfma_f32_32x32x64_f8f6f4 v[64:79], v[24:29], v[96:101], 0 cbsz:2 blgp:2
	ds_read_b128 v[0:3], v124 offset:12288
	ds_read_b128 v[4:7], v124 offset:13312
	ds_read_b128 v[8:11], v124 offset:14336
	ds_read_b128 v[24:27], v124 offset:18432
	v_mfma_f32_32x32x64_f8f6f4 v[64:79], v[30:35], v[102:107], v[64:79] cbsz:2 blgp:2
	ds_read_b128 v[12:15], v124 offset:15360
	ds_read_b128 v[16:19], v124 offset:16384
	ds_read_b128 v[20:23], v124 offset:17408
	ds_read_b128 v[28:31], v124 offset:19456
	ds_read_b128 v[32:35], v124 offset:20480
	v_exp_f32_e32 v48, v48
	v_exp_f32_e32 v49, v49
	v_exp_f32_e32 v50, v50
	v_exp_f32_e32 v51, v51
	v_mfma_f32_32x32x64_f8f6f4 v[64:79], v[36:41], v[108:113], v[64:79] cbsz:2 blgp:2
	ds_read_b128 v[36:39], v124 offset:21504
	v_exp_f32_e32 v52, v52
	v_exp_f32_e32 v53, v53
	v_exp_f32_e32 v54, v54
	v_exp_f32_e32 v55, v55
	v_pk_add_f32 v[120:121], v[120:121], v[48:49]
	v_pk_add_f32 v[122:123], v[122:123], v[50:51]
	v_mfma_f32_32x32x64_f8f6f4 v[64:79], v[42:47], v[114:119], v[64:79] cbsz:2 blgp:2
	ds_read_b128 v[40:43], v124 offset:22528
	ds_read_b128 v[44:47], v124 offset:23552
	v_exp_f32_e32 v56, v56
	v_exp_f32_e32 v57, v57
	v_exp_f32_e32 v58, v58
	v_exp_f32_e32 v59, v59
	v_pk_add_f32 v[120:121], v[120:121], v[52:53]
	v_pk_add_f32 v[122:123], v[122:123], v[54:55]
	s_waitcnt lgkmcnt(5)
	v_mfma_f32_32x32x64_f8f6f4 v[80:95], v[0:5], v[96:101], 0 cbsz:2 blgp:2
	ds_read_b128 v[0:3], v124 offset:24576
	v_exp_f32_e32 v60, v60
	v_exp_f32_e32 v61, v61
	v_exp_f32_e32 v62, v62
	v_exp_f32_e32 v63, v63
	v_pk_add_f32 v[120:121], v[120:121], v[56:57]
	v_pk_add_f32 v[122:123], v[122:123], v[58:59]
	v_mfma_f32_32x32x64_f8f6f4 v[80:95], v[6:11], v[102:107], v[80:95] cbsz:2 blgp:2
	ds_read_b128 v[4:7], v124 offset:25600
	ds_read_b128 v[8:11], v124 offset:26624
	v_exp_f32_e32 v64, v64
	v_exp_f32_e32 v65, v65
	v_exp_f32_e32 v66, v66
	v_exp_f32_e32 v67, v67
	v_pk_add_f32 v[120:121], v[120:121], v[60:61]
	v_pk_add_f32 v[122:123], v[122:123], v[62:63]
	v_mfma_f32_32x32x64_f8f6f4 v[80:95], v[12:17], v[108:113], v[80:95] cbsz:2 blgp:2
	ds_read_b128 v[12:15], v124 offset:27648
	v_exp_f32_e32 v68, v68
	v_exp_f32_e32 v69, v69
	v_exp_f32_e32 v70, v70
	v_exp_f32_e32 v71, v71
	v_pk_add_f32 v[120:121], v[120:121], v[64:65]
	v_pk_add_f32 v[122:123], v[122:123], v[66:67]
	v_mfma_f32_32x32x64_f8f6f4 v[80:95], v[18:23], v[114:119], v[80:95] cbsz:2 blgp:2
	ds_read_b128 v[16:19], v124 offset:28672
	ds_read_b128 v[20:23], v124 offset:29696
	v_exp_f32_e32 v72, v72
	v_exp_f32_e32 v73, v73
	v_exp_f32_e32 v74, v74
	v_exp_f32_e32 v75, v75
	v_pk_add_f32 v[120:121], v[120:121], v[68:69]
	v_pk_add_f32 v[122:123], v[122:123], v[70:71]
	s_waitcnt lgkmcnt(6)
	v_mfma_f32_32x32x64_f8f6f4 v[48:63], v[24:29], v[96:101], 0 cbsz:2 blgp:2
	ds_read_b128 v[24:27], v124 offset:30720
	v_exp_f32_e32 v76, v76
	v_exp_f32_e32 v77, v77
	v_exp_f32_e32 v78, v78
	v_exp_f32_e32 v79, v79
	v_pk_add_f32 v[120:121], v[120:121], v[72:73]
	v_pk_add_f32 v[122:123], v[122:123], v[74:75]
	v_mfma_f32_32x32x64_f8f6f4 v[48:63], v[30:35], v[102:107], v[48:63] cbsz:2 blgp:2
	ds_read_b128 v[28:31], v124 offset:31744
	ds_read_b128 v[32:35], v124 offset:32768
	v_exp_f32_e32 v80, v80
	v_exp_f32_e32 v81, v81
	v_exp_f32_e32 v82, v82
	v_exp_f32_e32 v83, v83
	v_pk_add_f32 v[120:121], v[120:121], v[76:77]
	v_pk_add_f32 v[122:123], v[122:123], v[78:79]
	v_mfma_f32_32x32x64_f8f6f4 v[48:63], v[36:41], v[108:113], v[48:63] cbsz:2 blgp:2
	ds_read_b128 v[36:39], v124 offset:33792
	v_exp_f32_e32 v84, v84
	v_exp_f32_e32 v85, v85
	v_exp_f32_e32 v86, v86
	v_exp_f32_e32 v87, v87
	v_pk_add_f32 v[120:121], v[120:121], v[80:81]
	v_pk_add_f32 v[122:123], v[122:123], v[82:83]
	v_mfma_f32_32x32x64_f8f6f4 v[48:63], v[42:47], v[114:119], v[48:63] cbsz:2 blgp:2
	ds_read_b128 v[40:43], v124 offset:34816
	ds_read_b128 v[44:47], v124 offset:35840
	v_exp_f32_e32 v88, v88
	v_exp_f32_e32 v89, v89
	v_exp_f32_e32 v90, v90
	v_exp_f32_e32 v91, v91
	v_pk_add_f32 v[120:121], v[120:121], v[84:85]
	v_pk_add_f32 v[122:123], v[122:123], v[86:87]
	s_setprio 2
	s_waitcnt lgkmcnt(6)
	v_mfma_f32_32x32x64_f8f6f4 v[64:79], v[0:5], v[96:101], 0 cbsz:2 blgp:2
	ds_read_b128 v[0:3], v124 offset:36864
	v_exp_f32_e32 v92, v92
	v_exp_f32_e32 v93, v93
	v_exp_f32_e32 v94, v94
	v_exp_f32_e32 v95, v95
	v_pk_add_f32 v[120:121], v[120:121], v[88:89]
	v_pk_add_f32 v[122:123], v[122:123], v[90:91]
	v_mfma_f32_32x32x64_f8f6f4 v[64:79], v[6:11], v[102:107], v[64:79] cbsz:2 blgp:2
	ds_read_b128 v[4:7], v124 offset:37888
	ds_read_b128 v[8:11], v124 offset:38912
	v_exp_f32_e32 v48, v48
	v_exp_f32_e32 v49, v49
	v_exp_f32_e32 v50, v50
	v_exp_f32_e32 v51, v51
	v_pk_add_f32 v[120:121], v[120:121], v[92:93]
	v_pk_add_f32 v[122:123], v[122:123], v[94:95]
	v_mfma_f32_32x32x64_f8f6f4 v[64:79], v[12:17], v[108:113], v[64:79] cbsz:2 blgp:2
	ds_read_b128 v[12:15], v124 offset:39936
	v_exp_f32_e32 v52, v52
	v_exp_f32_e32 v53, v53
	v_exp_f32_e32 v54, v54
	v_exp_f32_e32 v55, v55
	v_pk_add_f32 v[120:121], v[120:121], v[48:49]
	v_pk_add_f32 v[122:123], v[122:123], v[50:51]
	v_mfma_f32_32x32x64_f8f6f4 v[64:79], v[18:23], v[114:119], v[64:79] cbsz:2 blgp:2
	ds_read_b128 v[16:19], v124 offset:40960
	ds_read_b128 v[20:23], v124 offset:41984
	v_exp_f32_e32 v56, v56
	v_exp_f32_e32 v57, v57
	v_exp_f32_e32 v58, v58
	v_exp_f32_e32 v59, v59
	v_pk_add_f32 v[120:121], v[120:121], v[52:53]
	v_pk_add_f32 v[122:123], v[122:123], v[54:55]
	s_waitcnt lgkmcnt(6)
	v_mfma_f32_32x32x64_f8f6f4 v[80:95], v[24:29], v[96:101], 0 cbsz:2 blgp:2
	ds_read_b128 v[24:27], v124 offset:43008
	v_exp_f32_e32 v60, v60
	v_exp_f32_e32 v61, v61
	v_exp_f32_e32 v62, v62
	v_exp_f32_e32 v63, v63
	v_pk_add_f32 v[120:121], v[120:121], v[56:57]
	v_pk_add_f32 v[122:123], v[122:123], v[58:59]
	v_mfma_f32_32x32x64_f8f6f4 v[80:95], v[30:35], v[102:107], v[80:95] cbsz:2 blgp:2
	ds_read_b128 v[28:31], v124 offset:44032
	ds_read_b128 v[32:35], v124 offset:45056
	v_exp_f32_e32 v64, v64
	v_exp_f32_e32 v65, v65
	v_exp_f32_e32 v66, v66
	v_exp_f32_e32 v67, v67
	v_pk_add_f32 v[120:121], v[120:121], v[60:61]
	v_pk_add_f32 v[122:123], v[122:123], v[62:63]
	v_mfma_f32_32x32x64_f8f6f4 v[80:95], v[36:41], v[108:113], v[80:95] cbsz:2 blgp:2
	ds_read_b128 v[36:39], v124 offset:46080
	v_exp_f32_e32 v68, v68
	v_exp_f32_e32 v69, v69
	v_exp_f32_e32 v70, v70
	v_exp_f32_e32 v71, v71
	v_pk_add_f32 v[120:121], v[120:121], v[64:65]
	v_pk_add_f32 v[122:123], v[122:123], v[66:67]
	v_mfma_f32_32x32x64_f8f6f4 v[80:95], v[42:47], v[114:119], v[80:95] cbsz:2 blgp:2
	ds_read_b128 v[40:43], v124 offset:47104
	ds_read_b128 v[44:47], v124 offset:48128
	v_exp_f32_e32 v72, v72
	v_exp_f32_e32 v73, v73
	v_exp_f32_e32 v74, v74
	v_exp_f32_e32 v75, v75
	v_pk_add_f32 v[120:121], v[120:121], v[68:69]
	v_pk_add_f32 v[122:123], v[122:123], v[70:71]
	s_waitcnt lgkmcnt(6)
	v_mfma_f32_32x32x64_f8f6f4 v[48:63], v[0:5], v[96:101], 0 cbsz:2 blgp:2
	ds_read_b128 v[0:3], v124 offset:49152
	v_exp_f32_e32 v76, v76
	v_exp_f32_e32 v77, v77
	v_exp_f32_e32 v78, v78
	v_exp_f32_e32 v79, v79
	v_pk_add_f32 v[120:121], v[120:121], v[72:73]
	v_pk_add_f32 v[122:123], v[122:123], v[74:75]
	v_mfma_f32_32x32x64_f8f6f4 v[48:63], v[6:11], v[102:107], v[48:63] cbsz:2 blgp:2
	ds_read_b128 v[4:7], v124 offset:50176
	ds_read_b128 v[8:11], v124 offset:51200
	v_exp_f32_e32 v80, v80
	v_exp_f32_e32 v81, v81
	v_exp_f32_e32 v82, v82
	v_exp_f32_e32 v83, v83
	v_pk_add_f32 v[120:121], v[120:121], v[76:77]
	v_pk_add_f32 v[122:123], v[122:123], v[78:79]
	v_mfma_f32_32x32x64_f8f6f4 v[48:63], v[12:17], v[108:113], v[48:63] cbsz:2 blgp:2
	ds_read_b128 v[12:15], v124 offset:52224
	v_exp_f32_e32 v84, v84
	v_exp_f32_e32 v85, v85
	v_exp_f32_e32 v86, v86
	v_exp_f32_e32 v87, v87
	v_pk_add_f32 v[120:121], v[120:121], v[80:81]
	v_pk_add_f32 v[122:123], v[122:123], v[82:83]
	v_mfma_f32_32x32x64_f8f6f4 v[48:63], v[18:23], v[114:119], v[48:63] cbsz:2 blgp:2
	ds_read_b128 v[16:19], v124 offset:53248
	ds_read_b128 v[20:23], v124 offset:54272
	v_exp_f32_e32 v88, v88
	v_exp_f32_e32 v89, v89
	v_exp_f32_e32 v90, v90
	v_exp_f32_e32 v91, v91
	v_pk_add_f32 v[120:121], v[120:121], v[84:85]
	v_pk_add_f32 v[122:123], v[122:123], v[86:87]
	s_waitcnt lgkmcnt(6)
	v_mfma_f32_32x32x64_f8f6f4 v[64:79], v[24:29], v[96:101], 0 cbsz:2 blgp:2
	ds_read_b128 v[24:27], v124 offset:55296
	v_exp_f32_e32 v92, v92
	v_exp_f32_e32 v93, v93
	v_exp_f32_e32 v94, v94
	v_exp_f32_e32 v95, v95
	v_pk_add_f32 v[120:121], v[120:121], v[88:89]
	v_pk_add_f32 v[122:123], v[122:123], v[90:91]
	v_mfma_f32_32x32x64_f8f6f4 v[64:79], v[30:35], v[102:107], v[64:79] cbsz:2 blgp:2
	ds_read_b128 v[28:31], v124 offset:56320
	ds_read_b128 v[32:35], v124 offset:57344
	v_exp_f32_e32 v48, v48
	v_exp_f32_e32 v49, v49
	v_exp_f32_e32 v50, v50
	v_exp_f32_e32 v51, v51
	v_pk_add_f32 v[120:121], v[120:121], v[92:93]
	v_pk_add_f32 v[122:123], v[122:123], v[94:95]
	v_mfma_f32_32x32x64_f8f6f4 v[64:79], v[36:41], v[108:113], v[64:79] cbsz:2 blgp:2
	ds_read_b128 v[36:39], v124 offset:58368
	v_exp_f32_e32 v52, v52
	v_exp_f32_e32 v53, v53
	v_exp_f32_e32 v54, v54
	v_exp_f32_e32 v55, v55
	v_pk_add_f32 v[120:121], v[120:121], v[48:49]
	v_pk_add_f32 v[122:123], v[122:123], v[50:51]
	v_mfma_f32_32x32x64_f8f6f4 v[64:79], v[42:47], v[114:119], v[64:79] cbsz:2 blgp:2
	ds_read_b128 v[40:43], v124 offset:59392
	ds_read_b128 v[44:47], v124 offset:60416
	v_exp_f32_e32 v56, v56
	v_exp_f32_e32 v57, v57
	v_exp_f32_e32 v58, v58
	v_exp_f32_e32 v59, v59
	v_pk_add_f32 v[120:121], v[120:121], v[52:53]
	v_pk_add_f32 v[122:123], v[122:123], v[54:55]
	s_setprio 1
	s_waitcnt lgkmcnt(6)
	v_mfma_f32_32x32x64_f8f6f4 v[80:95], v[0:5], v[96:101], 0 cbsz:2 blgp:2
	ds_read_b128 v[0:3], v125
	v_exp_f32_e32 v60, v60
	v_exp_f32_e32 v61, v61
	v_exp_f32_e32 v62, v62
	v_exp_f32_e32 v63, v63
	v_pk_add_f32 v[120:121], v[120:121], v[56:57]
	v_pk_add_f32 v[122:123], v[122:123], v[58:59]
	v_mfma_f32_32x32x64_f8f6f4 v[80:95], v[6:11], v[102:107], v[80:95] cbsz:2 blgp:2
	ds_read_b128 v[4:7], v125 offset:1024
	ds_read_b128 v[8:11], v125 offset:2048
	v_exp_f32_e32 v64, v64
	v_exp_f32_e32 v65, v65
	v_exp_f32_e32 v66, v66
	v_exp_f32_e32 v67, v67
	v_pk_add_f32 v[120:121], v[120:121], v[60:61]
	v_pk_add_f32 v[122:123], v[122:123], v[62:63]
	v_mfma_f32_32x32x64_f8f6f4 v[80:95], v[12:17], v[108:113], v[80:95] cbsz:2 blgp:2
	ds_read_b128 v[12:15], v125 offset:3072
	v_exp_f32_e32 v68, v68
	v_exp_f32_e32 v69, v69
	v_exp_f32_e32 v70, v70
	v_exp_f32_e32 v71, v71
	v_pk_add_f32 v[120:121], v[120:121], v[64:65]
	v_pk_add_f32 v[122:123], v[122:123], v[66:67]
	v_mfma_f32_32x32x64_f8f6f4 v[80:95], v[18:23], v[114:119], v[80:95] cbsz:2 blgp:2
	ds_read_b128 v[16:19], v125 offset:4096
	ds_read_b128 v[20:23], v125 offset:5120
	v_exp_f32_e32 v72, v72
	v_exp_f32_e32 v73, v73
	v_exp_f32_e32 v74, v74
	v_exp_f32_e32 v75, v75
	v_pk_add_f32 v[120:121], v[120:121], v[68:69]
	v_pk_add_f32 v[122:123], v[122:123], v[70:71]
	s_waitcnt lgkmcnt(6)
	v_mfma_f32_32x32x64_f8f6f4 v[48:63], v[24:29], v[96:101], 0 cbsz:2 blgp:2
	ds_read_b128 v[24:27], v125 offset:6144
	v_exp_f32_e32 v76, v76
	v_exp_f32_e32 v77, v77
	v_exp_f32_e32 v78, v78
	v_exp_f32_e32 v79, v79
	v_pk_add_f32 v[120:121], v[120:121], v[72:73]
	v_pk_add_f32 v[122:123], v[122:123], v[74:75]
	v_mfma_f32_32x32x64_f8f6f4 v[48:63], v[30:35], v[102:107], v[48:63] cbsz:2 blgp:2
	ds_read_b128 v[28:31], v125 offset:7168
	ds_read_b128 v[32:35], v125 offset:8192
	v_exp_f32_e32 v80, v80
	v_exp_f32_e32 v81, v81
	v_exp_f32_e32 v82, v82
	v_exp_f32_e32 v83, v83
	v_pk_add_f32 v[120:121], v[120:121], v[76:77]
	v_pk_add_f32 v[122:123], v[122:123], v[78:79]
	s_cmp_lg_u32 s8, 10
	s_cbranch_scc1 .Lmk_nosplit_b
	v_add_f32_e32 v127, v120, v121
	v_add_f32_e32 v126, v122, v123
	v_mov_b32_e32 v120, 0
	v_mov_b32_e32 v121, 0
	v_mov_b32_e32 v122, 0
	v_mov_b32_e32 v123, 0
	v_add_f32_e32 v127, v127, v126
.Lmk_nosplit_b:
	v_mfma_f32_32x32x64_f8f6f4 v[48:63], v[36:41], v[108:113], v[48:63] cbsz:2 blgp:2
	ds_read_b128 v[36:39], v125 offset:9216
	v_exp_f32_e32 v84, v84
	v_exp_f32_e32 v85, v85
	v_exp_f32_e32 v86, v86
	v_exp_f32_e32 v87, v87
	v_pk_add_f32 v[120:121], v[120:121], v[80:81]
	v_pk_add_f32 v[122:123], v[122:123], v[82:83]
	v_mfma_f32_32x32x64_f8f6f4 v[48:63], v[42:47], v[114:119], v[48:63] cbsz:2 blgp:2
	ds_read_b128 v[40:43], v125 offset:10240
	ds_read_b128 v[44:47], v125 offset:11264
	v_exp_f32_e32 v88, v88
	v_exp_f32_e32 v89, v89
	v_exp_f32_e32 v90, v90
	v_exp_f32_e32 v91, v91
	v_pk_add_f32 v[120:121], v[120:121], v[84:85]
	v_pk_add_f32 v[122:123], v[122:123], v[86:87]
	s_setprio 0
	s_waitcnt lgkmcnt(6)
	v_mfma_f32_32x32x64_f8f6f4 v[64:79], v[0:5], v[96:101], 0 cbsz:2 blgp:2
	v_exp_f32_e32 v92, v92
	v_exp_f32_e32 v93, v93
	v_exp_f32_e32 v94, v94
	v_exp_f32_e32 v95, v95
	v_pk_add_f32 v[120:121], v[120:121], v[88:89]
	v_pk_add_f32 v[122:123], v[122:123], v[90:91]
	v_mfma_f32_32x32x64_f8f6f4 v[64:79], v[6:11], v[102:107], v[64:79] cbsz:2 blgp:2
	v_exp_f32_e32 v48, v48
	v_exp_f32_e32 v49, v49
	v_exp_f32_e32 v50, v50
	v_exp_f32_e32 v51, v51
	v_pk_add_f32 v[120:121], v[120:121], v[92:93]
	v_pk_add_f32 v[122:123], v[122:123], v[94:95]
	v_mfma_f32_32x32x64_f8f6f4 v[64:79], v[12:17], v[108:113], v[64:79] cbsz:2 blgp:2
	v_exp_f32_e32 v52, v52
	v_exp_f32_e32 v53, v53
	v_exp_f32_e32 v54, v54
	v_exp_f32_e32 v55, v55
	v_pk_add_f32 v[120:121], v[120:121], v[48:49]
	v_pk_add_f32 v[122:123], v[122:123], v[50:51]
	v_mfma_f32_32x32x64_f8f6f4 v[64:79], v[18:23], v[114:119], v[64:79] cbsz:2 blgp:2
	v_exp_f32_e32 v56, v56
	v_exp_f32_e32 v57, v57
	v_exp_f32_e32 v58, v58
	v_exp_f32_e32 v59, v59
	v_pk_add_f32 v[120:121], v[120:121], v[52:53]
	v_pk_add_f32 v[122:123], v[122:123], v[54:55]
	s_waitcnt lgkmcnt(0)
	v_mfma_f32_32x32x64_f8f6f4 v[80:95], v[24:29], v[96:101], 0 cbsz:2 blgp:2
	v_exp_f32_e32 v60, v60
	v_exp_f32_e32 v61, v61
	v_exp_f32_e32 v62, v62
	v_exp_f32_e32 v63, v63
	v_pk_add_f32 v[120:121], v[120:121], v[56:57]
	v_pk_add_f32 v[122:123], v[122:123], v[58:59]
	v_mfma_f32_32x32x64_f8f6f4 v[80:95], v[30:35], v[102:107], v[80:95] cbsz:2 blgp:2
	v_exp_f32_e32 v64, v64
	v_exp_f32_e32 v65, v65
	v_exp_f32_e32 v66, v66
	v_exp_f32_e32 v67, v67
	v_pk_add_f32 v[120:121], v[120:121], v[60:61]
	v_pk_add_f32 v[122:123], v[122:123], v[62:63]
	v_mfma_f32_32x32x64_f8f6f4 v[80:95], v[36:41], v[108:113], v[80:95] cbsz:2 blgp:2
	v_exp_f32_e32 v68, v68
	v_exp_f32_e32 v69, v69
	v_exp_f32_e32 v70, v70
	v_exp_f32_e32 v71, v71
	v_pk_add_f32 v[120:121], v[120:121], v[64:65]
	v_pk_add_f32 v[122:123], v[122:123], v[66:67]
	v_mfma_f32_32x32x64_f8f6f4 v[80:95], v[42:47], v[114:119], v[80:95] cbsz:2 blgp:2
	v_exp_f32_e32 v72, v72
	v_exp_f32_e32 v73, v73
	v_exp_f32_e32 v74, v74
	v_exp_f32_e32 v75, v75
	v_pk_add_f32 v[120:121], v[120:121], v[68:69]
	v_pk_add_f32 v[122:123], v[122:123], v[70:71]
	v_exp_f32_e32 v76, v76
	v_exp_f32_e32 v77, v77
	v_exp_f32_e32 v78, v78
	v_exp_f32_e32 v79, v79
	v_pk_add_f32 v[120:121], v[120:121], v[72:73]
	v_pk_add_f32 v[122:123], v[122:123], v[74:75]
	s_nop 1
	v_exp_f32_e32 v80, v80
	v_exp_f32_e32 v81, v81
	v_exp_f32_e32 v82, v82
	v_exp_f32_e32 v83, v83
	v_pk_add_f32 v[120:121], v[120:121], v[76:77]
	v_pk_add_f32 v[122:123], v[122:123], v[78:79]
	v_exp_f32_e32 v84, v84
	v_exp_f32_e32 v85, v85
	v_exp_f32_e32 v86, v86
	v_exp_f32_e32 v87, v87
	v_pk_add_f32 v[120:121], v[120:121], v[80:81]
	v_pk_add_f32 v[122:123], v[122:123], v[82:83]
	v_exp_f32_e32 v88, v88
	v_exp_f32_e32 v89, v89
	v_exp_f32_e32 v90, v90
	v_exp_f32_e32 v91, v91
	v_pk_add_f32 v[120:121], v[120:121], v[84:85]
	v_pk_add_f32 v[122:123], v[122:123], v[86:87]
	v_exp_f32_e32 v92, v92
	v_exp_f32_e32 v93, v93
	v_exp_f32_e32 v94, v94
	v_exp_f32_e32 v95, v95
	v_pk_add_f32 v[120:121], v[120:121], v[88:89]
	v_pk_add_f32 v[122:123], v[122:123], v[90:91]
	v_pk_add_f32 v[120:121], v[120:121], v[92:93]
	v_pk_add_f32 v[122:123], v[122:123], v[94:95]
	v_add_f32_e32 v120, v120, v121
	v_add_f32_e32 v122, v122, v123
	v_lshrrev_b32_e32 v126, 2, v124
	v_add_f32_e32 v120, v120, v122
	v_mov_b32_e32 v123, v127
	v_mov_b32_e32 v122, v120
	s_mov_b64 s[4:5], s[30:31]
	s_mov_b64 s[6:7], s[32:33]
	s_lshl_b32 s14, s14, 7
	v_add_u32_e32 v126, s14, v126
	s_nop 1
	v_permlane32_swap_b32_e32 v120, v122
	v_permlane32_swap_b32_e32 v127, v123
	s_nop 1
	v_add_f32_e32 v120, v120, v122
	v_add_f32_e32 v127, v127, v123
	v_cmp_gt_u32_e32 vcc, 0x200, v124
	s_and_saveexec_b64 s[16:17], vcc
	s_cbranch_execz .Lmk_end_b
	s_cmp_lt_u32 s8, 10
	s_cbranch_scc1 .Lmk_pos_only_b
	s_cmp_eq_u32 s8, 10
	s_cbranch_scc0 .Lmk_neg_only_b
	global_atomic_add_f32 v126, v127, s[4:5]

	.amdhsa_kernel _Z11main_kernelPKcPfS1_
		.amdhsa_group_segment_fixed_size 73728
		.amdhsa_private_segment_fixed_size 0
		.amdhsa_kernarg_size 24
		.amdhsa_user_sgpr_count 8
		.amdhsa_user_sgpr_dispatch_ptr 0
		.amdhsa_user_sgpr_queue_ptr 0
		.amdhsa_user_sgpr_kernarg_segment_ptr 1
		.amdhsa_user_sgpr_dispatch_id 0
		.amdhsa_user_sgpr_kernarg_preload_length 6
		.amdhsa_user_sgpr_kernarg_preload_offset 0
		.amdhsa_user_sgpr_private_segment_size 0
		.amdhsa_uses_dynamic_stack 0
		.amdhsa_enable_private_segment 0
		.amdhsa_system_sgpr_workgroup_id_x 1
		.amdhsa_system_sgpr_workgroup_id_y 0
		.amdhsa_system_sgpr_workgroup_id_z 0
		.amdhsa_system_sgpr_workgroup_info 0
		.amdhsa_system_vgpr_workitem_id 0
		.amdhsa_next_free_vgpr 128
		.amdhsa_next_free_sgpr 96
		.amdhsa_accum_offset 128
		.amdhsa_reserve_vcc 1
		.amdhsa_float_round_mode_32 0
		.amdhsa_float_round_mode_16_64 0
		.amdhsa_float_denorm_mode_32 3
		.amdhsa_float_denorm_mode_16_64 3
		.amdhsa_dx10_clamp 1
		.amdhsa_ieee_mode 1
		.amdhsa_fp16_overflow 0
		.amdhsa_tg_split 0
		.amdhsa_exception_fp_ieee_invalid_op 0
		.amdhsa_exception_fp_denorm_src 0
		.amdhsa_exception_fp_ieee_div_zero 0
		.amdhsa_exception_fp_ieee_overflow 0
		.amdhsa_exception_fp_ieee_underflow 0
		.amdhsa_exception_fp_ieee_inexact 0
		.amdhsa_exception_int_div_zero 0
	.end_amdhsa_kernel

amdhsa.kernels:
  - .agpr_count:     0
    .args:
      - .actual_access:  read_only
        .address_space:  global
        .offset:         0
        .size:           8
        .value_kind:     global_buffer
      - .actual_access:  read_only
        .address_space:  global
        .offset:         8
        .size:           8
        .value_kind:     global_buffer
      - .actual_access:  read_only
        .address_space:  global
        .offset:         16
        .size:           8
        .value_kind:     global_buffer
      - .actual_access:  write_only
        .address_space:  global
        .offset:         24
        .size:           8
        .value_kind:     global_buffer
      - .actual_access:  write_only
        .address_space:  global
        .offset:         32
        .size:           8
        .value_kind:     global_buffer
      - .actual_access:  write_only
        .address_space:  global
        .offset:         40
        .size:           8
        .value_kind:     global_buffer
      - .actual_access:  write_only
        .address_space:  global
        .offset:         48
        .size:           8
        .value_kind:     global_buffer
      - .actual_access:  write_only
        .address_space:  global
        .offset:         56
        .size:           8
        .value_kind:     global_buffer
    .group_segment_fixed_size: 36864
    .kernarg_segment_align: 8
    .kernarg_segment_size: 64
    .language:       OpenCL C
    .language_version:
      - 2
      - 0
    .max_flat_workgroup_size: 1024
    .name:           _Z11prep_kernelPKfS0_S0_PcPfS2_S2_S2_
    .private_segment_fixed_size: 0
    .sgpr_count:     38
    .sgpr_spill_count: 0
    .symbol:         _Z11prep_kernelPKfS0_S0_PcPfS2_S2_S2_.kd
    .uniform_work_group_size: 1
    .uses_dynamic_stack: false
    .vgpr_count:     64
    .vgpr_spill_count: 0
    .wavefront_size: 64
  - .agpr_count:     0
    .args:
      - .address_space:  global
        .offset:         0
        .size:           8
        .value_kind:     global_buffer
      - .address_space:  global
        .offset:         8
        .size:           8
        .value_kind:     global_buffer
      - .address_space:  global
        .offset:         16
        .size:           8
        .value_kind:     global_buffer
    .group_segment_fixed_size: 73728
    .kernarg_segment_align: 8
    .kernarg_segment_size: 24
    .language:       OpenCL C
    .language_version:
      - 2
      - 0
    .max_flat_workgroup_size: 512
    .name:           _Z11main_kernelPKcPfS1_
    .private_segment_fixed_size: 0
    .sgpr_count:     34
    .sgpr_spill_count: 0
    .symbol:         _Z11main_kernelPKcPfS1_.kd
    .uniform_work_group_size: 1
    .uses_dynamic_stack: false
    .vgpr_count:     128
    .vgpr_spill_count: 0
    .wavefront_size: 64
  - .agpr_count:     0
    .args:
      - .actual_access:  read_only
        .address_space:  global
        .offset:         0
        .size:           8
        .value_kind:     global_buffer
      - .actual_access:  read_only
        .address_space:  global
        .offset:         8
        .size:           8
        .value_kind:     global_buffer
      - .actual_access:  read_only
        .address_space:  global
        .offset:         16
        .size:           8
        .value_kind:     global_buffer
      - .actual_access:  read_only
        .address_space:  global
        .offset:         24
        .size:           8
        .value_kind:     global_buffer
      - .address_space:  global
        .offset:         32
        .size:           8
        .value_kind:     global_buffer
    .group_segment_fixed_size: 2064
    .kernarg_segment_align: 8
    .kernarg_segment_size: 40
    .language:       OpenCL C
    .language_version:
      - 2
      - 0
    .max_flat_workgroup_size: 256
    .name:           _Z12final_kernelPKfS0_S0_S0_Pf
    .private_segment_fixed_size: 0
    .sgpr_count:     26
    .sgpr_spill_count: 0
    .symbol:         _Z12final_kernelPKfS0_S0_S0_Pf.kd
    .uniform_work_group_size: 1
    .uses_dynamic_stack: false
    .vgpr_count:     36
    .vgpr_spill_count: 0
    .wavefront_size: 64
